# gcn2: block-uniform predicate of __syncthreads_and evaluated directly (drops DPP/LDS reduction and 3 extra barriers)
# speedup vs baseline: 1.0024x; 1.0024x over previous
.LBB5_9:
	s_or_b64 exec, exec, s[4:5]
	v_and_b32_e32 v3, 0x3c0, v78
	v_add_u32_e32 v2, 0x5800, v3
	s_movk_i32 s6, 0x200
	s_load_dwordx2 s[24:25], s[0:1], 0x60
	s_waitcnt lgkmcnt(0)
	s_barrier
	ds_read2_b32 v[64:65], v2 offset0:64 offset1:79
	ds_read_b32 v2, v3 offset:23100
	v_cmp_lt_i32_e64 s[0:1], s6, v1
	s_movk_i32 s6, 0x201
	v_cmp_gt_i32_e32 vcc, s6, v1
	v_lshrrev_b32_e32 v79, 6, v78
	v_mbcnt_lo_u32_b32 v81, -1, 0
	v_cndmask_b32_e64 v1, 0, 1, vcc
	s_waitcnt lgkmcnt(0)
